# K3 count phase straight-line with address reuse in msplit; K1 loads via buffer descriptors with immediate offsets
# baseline (speedup 1.0000x reference)
.LBB0_7:
	v_add_u32_e32 v1, 0x400, v1
	v_cmp_lt_u32_e32 vcc, s3, v1
	ds_write2st64_b32 v2, v3, v3 offset1:64
	s_or_b64 s[0:1], vcc, s[0:1]
	v_add_u32_e32 v2, 0x1000, v2
	s_andn2_b64 exec, exec, s[0:1]
	s_cbranch_execnz .LBB0_7
	s_or_b64 exec, exec, s[0:1]
	s_mul_i32 s34, s2, 0x30d4
	v_lshrrev_b32_e32 v53, 6, v0
	v_and_b32_e32 v2, 63, v0
	v_mov_b32_e32 v60, 0
	v_mov_b32_e32 v78, 0
	v_mov_b32_e32 v79, 0
	v_readfirstlane_b32 s50, v53
	s_mul_i32 s51, s50, 0x30e
	s_add_i32 s51, s51, s34
	s_add_i32 s49, s34, 0x30d4
	s_sub_i32 s49, s49, s51
	s_min_u32 s49, s49, 0x30e
	v_add_u32_e32 v3, s51, v2
	v_lshlrev_b32_e32 v3, 2, v3
	s_waitcnt lgkmcnt(0)
	s_mov_b32 s52, s28
	s_and_b32 s53, s29, 0xffff
	s_mov_b32 s54, 0xc35000
	s_mov_b32 s55, 0x20000
	s_mov_b32 s56, s30
	s_and_b32 s57, s31, 0xffff
	s_mov_b32 s58, 0xc35000
	s_mov_b32 s59, 0x20000
	buffer_load_dword v52, v3, s[56:59], 0 offen nt
	buffer_load_dword v51, v3, s[52:55], 0 offen nt
	v_cmp_gt_i32_e64 s[22:23], s49, v2
	s_sub_i32 s49, s49, 64
	buffer_load_dword v50, v3, s[56:59], 0 offen offset:256 nt
	buffer_load_dword v49, v3, s[52:55], 0 offen offset:256 nt
	v_cmp_gt_i32_e64 s[20:21], s49, v2
	s_sub_i32 s49, s49, 64
	buffer_load_dword v48, v3, s[56:59], 0 offen offset:512 nt
	buffer_load_dword v47, v3, s[52:55], 0 offen offset:512 nt
	v_cmp_gt_i32_e64 s[18:19], s49, v2
	s_sub_i32 s49, s49, 64
	buffer_load_dword v46, v3, s[56:59], 0 offen offset:768 nt
	buffer_load_dword v45, v3, s[52:55], 0 offen offset:768 nt
	v_cmp_gt_i32_e64 s[16:17], s49, v2
	s_sub_i32 s49, s49, 64
	buffer_load_dword v44, v3, s[56:59], 0 offen offset:1024 nt
	buffer_load_dword v43, v3, s[52:55], 0 offen offset:1024 nt
	v_cmp_gt_i32_e64 s[14:15], s49, v2
	s_sub_i32 s49, s49, 64
	buffer_load_dword v42, v3, s[56:59], 0 offen offset:1280 nt
	buffer_load_dword v41, v3, s[52:55], 0 offen offset:1280 nt
	v_cmp_gt_i32_e64 s[12:13], s49, v2
	s_sub_i32 s49, s49, 64
	buffer_load_dword v40, v3, s[56:59], 0 offen offset:1536 nt
	buffer_load_dword v39, v3, s[52:55], 0 offen offset:1536 nt
	v_cmp_gt_i32_e64 s[10:11], s49, v2
	s_sub_i32 s49, s49, 64
	buffer_load_dword v38, v3, s[56:59], 0 offen offset:1792 nt
	buffer_load_dword v37, v3, s[52:55], 0 offen offset:1792 nt
	v_cmp_gt_i32_e64 s[8:9], s49, v2
	s_sub_i32 s49, s49, 64
	buffer_load_dword v36, v3, s[56:59], 0 offen offset:2048 nt
	buffer_load_dword v35, v3, s[52:55], 0 offen offset:2048 nt
	v_cmp_gt_i32_e64 s[6:7], s49, v2
	s_sub_i32 s49, s49, 64
	buffer_load_dword v34, v3, s[56:59], 0 offen offset:2304 nt
	buffer_load_dword v33, v3, s[52:55], 0 offen offset:2304 nt
	v_cmp_gt_i32_e64 s[4:5], s49, v2
	s_sub_i32 s49, s49, 64
	buffer_load_dword v32, v3, s[56:59], 0 offen offset:2560 nt
	buffer_load_dword v31, v3, s[52:55], 0 offen offset:2560 nt
	v_cmp_gt_i32_e64 s[24:25], s49, v2
	s_sub_i32 s49, s49, 64
	buffer_load_dword v30, v3, s[56:59], 0 offen offset:2816 nt
	buffer_load_dword v28, v3, s[52:55], 0 offen offset:2816 nt
	v_cmp_gt_i32_e64 s[0:1], s49, v2
	s_sub_i32 s49, s49, 64
	buffer_load_dword v1, v3, s[52:55], 0 offen offset:3072 nt
	buffer_load_dword v26, v3, s[56:59], 0 offen offset:3072 nt
	v_cmp_gt_i32_e32 vcc, s49, v2
	v_lshlrev_b32_e32 v3, 10, v53
	v_add_u32_e32 v27, 0x12500, v3
	v_add_u32_e32 v29, 0x16500, v3
	s_barrier
	s_and_saveexec_b64 s[26:27], s[22:23]
	s_cbranch_execz .LBB0_10
	s_mov_b32 s3, 0x51eb851f
	s_waitcnt vmcnt(25)
	v_mul_hi_u32 v3, v52, s3
	v_lshrrev_b32_e32 v3, 5, v3
	v_and_b32_e32 v3, 0x3fffffc, v3
	v_add_u32_e32 v3, v27, v3
	v_mov_b32_e32 v4, 1
	ds_add_rtn_u32 v78, v3, v4
	s_waitcnt vmcnt(24)
	v_mul_hi_u32 v3, v51, s3
	v_lshrrev_b32_e32 v3, 5, v3
	v_and_b32_e32 v3, 0x3fffffc, v3
	v_add_u32_e32 v3, v29, v3
	ds_add_rtn_u32 v79, v3, v4
